# speedup vs baseline: 1.0035x; 1.0035x over previous
_Z7k_fusedPKfS0_S0_S0_S0_S0_S0_S0_S0_S0_S0_S0_S0_S0_PfS1_:
	s_load_dwordx2 s[34:35], s[0:1], 0x70
	s_load_dwordx2 s[60:61], s[0:1], 0x0
	s_load_dwordx4 s[20:23], s[0:1], 0x60
	s_load_dwordx4 s[24:27], s[0:1], 0x40
	s_load_dwordx4 s[28:31], s[0:1], 0x10
	s_and_b32 s33, s2, 7
	s_ashr_i32 s36, s2, 3
	s_cmp_lt_i32 s36, 31
	s_mov_b64 s[2:3], -1
	s_cbranch_scc1 .LBB5_52
	s_endpgm
	s_mul_i32 s11, s33, 0x1cc8
	v_add_u32_e32 v1, s11, v0
	v_lshlrev_b32_e32 v22, 4, v1
	v_mov_b32_e32 v23, 0
	s_add_i32 s8, s11, 0x1cc8
	s_add_i32 s9, s11, 0x1a48
	s_add_i32 s10, s11, 0x17c8
	s_addk_i32 s11, 0x1548
	s_waitcnt lgkmcnt(0)
	v_lshl_add_u64 v[24:25], s[28:29], 0, v[22:23]
	s_mov_b64 s[2:3], 0
	s_mov_b64 s[4:5], 0xa000
	v_mov_b32_e32 v26, v1
	v_mov_b32_e32 v18, v23
	v_mov_b32_e32 v19, v23
	v_mov_b32_e32 v20, v23
	v_mov_b32_e32 v21, v23
	s_branch .LBB5_3

.LBB5_55:
	s_load_dwordx8 s[12:19], s[2:3], 0x4
	s_load_dword s49, s[2:3], 0x24
	s_mul_i32 s59, s33, 0x133
	s_add_i32 s59, s59, s37
	s_mul_i32 s62, s59, 0xc00
	s_add_u32 s62, s60, s62
	s_addc_u32 s63, s61, 0
	v_and_b32_e32 v87, 63, v0
	v_lshlrev_b32_e32 v87, 4, v87
	global_load_dwordx4 v[22:25], v87, s[62:63]
	global_load_dwordx4 v[62:65], v87, s[62:63] offset:1024
	global_load_dwordx4 v[66:69], v87, s[62:63] offset:2048
	s_add_u32 s42, s34, 0x125000
	s_addc_u32 s43, s35, 0
	v_lshlrev_b32_e32 v78, 4, v0
	global_load_dwordx4 v[2:5], v78, s[42:43]
	s_load_dwordx2 s[4:5], s[0:1], 0x28
	v_mov_b32_e32 v79, 0
	s_movk_i32 s6, 0x80
	v_lshl_add_u64 v[84:85], s[42:43], 0, v[78:79]
	v_cmp_gt_u32_e64 s[10:11], s6, v0
	s_and_saveexec_b64 s[6:7], s[10:11]
	s_cbranch_execz .LBB5_57
	v_add_co_u32_e32 v6, vcc, 0x2000, v84
	s_nop 1
	v_addc_co_u32_e32 v7, vcc, 0, v85, vcc
	global_load_dwordx4 v[6:9], v[6:7], off offset:2048

.LBB5_73:
	s_or_b64 exec, exec, s[38:39]
	s_mul_i32 s38, s33, 0x133
	s_ashr_i32 s39, s37, 31
	s_add_u32 s40, s37, s38
	s_addc_u32 s39, s39, 0
	s_mulk_i32 s39, 0xc00
	s_mul_hi_u32 s41, s40, 0xc00
	s_add_i32 s41, s41, s39
	s_mulk_i32 s40, 0xc00
	s_waitcnt lgkmcnt(0)
	s_add_u32 s40, s6, s40
	s_addc_u32 s41, s7, s41
	s_ashr_i32 s39, s12, 31
	s_add_u32 s12, s12, s38
	s_addc_u32 s39, s39, 0
	s_mulk_i32 s39, 0xc00
	s_mul_hi_u32 s46, s12, 0xc00
	s_add_i32 s46, s46, s39
	s_mulk_i32 s12, 0xc00
	s_add_u32 s50, s6, s12
	s_addc_u32 s51, s7, s46
	s_ashr_i32 s12, s13, 31
	s_add_u32 s13, s13, s38
	s_addc_u32 s12, s12, 0
	s_mulk_i32 s12, 0xc00
	s_mul_hi_u32 s39, s13, 0xc00
	s_add_i32 s39, s39, s12
	s_mulk_i32 s13, 0xc00
	s_add_u32 s12, s6, s13
	s_addc_u32 s13, s7, s39
	s_ashr_i32 s39, s14, 31
	s_add_u32 s14, s14, s38
	v_lshlrev_b32_e32 v80, 4, v128
	s_addc_u32 s39, s39, 0
	global_load_dwordx4 v[50:53], v80, s[50:51]
	global_load_dwordx4 v[54:57], v80, s[50:51] offset:1024
	global_load_dwordx4 v[58:61], v80, s[50:51] offset:2048
	s_mulk_i32 s39, 0xc00
	s_mul_hi_u32 s40, s14, 0xc00
	s_add_i32 s39, s40, s39
	s_mulk_i32 s14, 0xc00
	s_add_u32 s40, s6, s14
	global_load_dwordx4 v[38:41], v80, s[12:13]
	global_load_dwordx4 v[42:45], v80, s[12:13] offset:1024
	s_addc_u32 s41, s7, s39
	global_load_dwordx4 v[46:49], v80, s[12:13] offset:2048
	global_load_dwordx4 v[26:29], v80, s[40:41]
	global_load_dwordx4 v[30:33], v80, s[40:41] offset:1024
	global_load_dwordx4 v[34:37], v80, s[40:41] offset:2048
	s_mov_b32 s39, 0
	s_waitcnt vmcnt(9)
	ds_write_b128 v78, v[2:5]
	s_and_saveexec_b64 s[12:13], s[10:11]
	s_cbranch_execz .LBB5_75
	s_waitcnt vmcnt(9)
	ds_write_b128 v78, v[6:9] offset:10240
.LBB5_75:
	s_or_b64 exec, exec, s[12:13]
	s_movk_i32 s12, 0x48
	v_cmp_gt_u32_e32 vcc, s12, v0
	s_and_saveexec_b64 s[12:13], vcc
	s_cbranch_execz .LBB5_77
	v_mov_b32_e32 v2, 0x23d00
	v_lshl_add_u32 v2, v0, 2, v2
	s_waitcnt vmcnt(9)
	ds_write_b32 v2, v1
.LBB5_77:
	s_or_b64 exec, exec, s[12:13]
	s_and_saveexec_b64 s[12:13], s[4:5]
	s_cbranch_execz .LBB5_79
	s_waitcnt vmcnt(9)
	v_mov_b32_e32 v1, 0x23900
	v_mul_f32_e32 v14, v14, v86
	v_lshl_add_u32 v1, v0, 2, v1
	ds_write_b32 v1, v14
.LBB5_79:
	s_or_b64 exec, exec, s[12:13]
	s_movk_i32 s12, 0x140
	v_cmp_gt_u32_e32 vcc, s12, v0
	s_and_saveexec_b64 s[12:13], vcc
	s_cbranch_execz .LBB5_81
	s_waitcnt vmcnt(9)
	v_mov_b32_e32 v1, 0x23400
	v_lshl_add_u32 v1, v0, 2, v1
	ds_write_b32 v1, v15
.LBB5_81:
	s_or_b64 exec, exec, s[12:13]
	s_and_saveexec_b64 s[12:13], s[2:3]
	s_cbranch_execz .LBB5_83
	s_waitcnt vmcnt(9)
	v_mov_b32_e32 v1, 0x22800
	v_pk_add_f32 v[12:13], v[12:13], v[18:19]
	v_pk_add_f32 v[10:11], v[10:11], v[16:17]
	v_lshl_add_u32 v1, v0, 4, v1
	ds_write_b128 v1, v[10:13]
.LBB5_83:
	s_or_b64 exec, exec, s[12:13]
	s_load_dwordx2 s[40:41], s[0:1], 0x78
	v_lshrrev_b32_e32 v126, 4, v128
	v_and_b32_e32 v127, 15, v0
	s_waitcnt vmcnt(9)
	v_mul_u32_u24_e32 v1, 48, v126
	s_waitcnt lgkmcnt(0)
	s_barrier
	v_or_b32_e32 v129, v1, v127
	s_mul_i32 s46, s45, 0xc00
	v_cmp_gt_u32_e64 s[2:3], 12, v127
	v_cndmask_b32_e64 v1, 0, 1, s[8:9]
	v_lshlrev_b32_e32 v131, 2, v126
	s_add_i32 s46, s46, 0x1b000
	v_mov_b32_e32 v71, 0
	v_cndmask_b32_e64 v130, 0, 1.0, s[2:3]
	v_cmp_ne_u32_e64 s[0:1], 1, v1
	s_andn2_b64 vcc, exec, s[8:9]
	v_add_u32_e32 v79, -8, v129
	v_mov_b32_e32 v70, 0
	s_cbranch_vccnz .Lmy_inact93
	v_cndmask_b32_e64 v1, v79, v129, s[2:3]
	v_lshlrev_b32_e32 v81, 2, v1
	v_add_u32_e32 v1, 0x22800, v81
	ds_read2_b32 v[6:7], v1 offset1:12
	ds_read2_b32 v[8:9], v1 offset0:24 offset1:36
	ds_read2_b32 v[10:11], v1 offset0:192 offset1:204
	ds_read2_b32 v[12:13], v1 offset0:216 offset1:228
	v_add_u32_e32 v2, 0x400, v1
	v_add_u32_e32 v1, 0x800, v1
	ds_read2_b32 v[14:15], v2 offset0:128 offset1:140
	ds_read2_b32 v[16:17], v2 offset0:152 offset1:164
	ds_read2_b32 v[70:71], v1 offset0:64 offset1:76
	ds_read_b128 v[2:5], v80
	ds_read2_b32 v[72:73], v1 offset0:88 offset1:100
	s_waitcnt lgkmcnt(0)
	v_cvt_pk_bf16_f32 v18, v6, v7
	v_cvt_pk_bf16_f32 v19, v8, v9
	ds_read_b128 v[6:9], v80 offset:1024
	v_cvt_pk_bf16_f32 v20, v10, v11
	v_cvt_pk_bf16_f32 v21, v12, v13
	ds_read_b128 v[10:13], v80 offset:2048
	v_cvt_pk_bf16_f32 v86, v14, v15
	v_mfma_f32_16x16x32_bf16 v[2:5], v[2:5], v[18:21], 0
	v_cvt_pk_bf16_f32 v87, v16, v17
	v_cvt_pk_bf16_f32 v88, v70, v71
	v_cvt_pk_bf16_f32 v89, v72, v73
	ds_read_b128 v[70:73], v80 offset:4096
	v_mov_b32_e32 v1, 0x23e00
	s_waitcnt lgkmcnt(2)
	v_mfma_f32_16x16x32_bf16 v[14:17], v[6:9], v[86:89], v[2:5]
	v_add_u32_e32 v96, s46, v81
	s_cmp_lt_i32 s48, 1
	ds_read_b128 v[74:77], v80 offset:6144
	ds_read_b128 v[2:5], v80 offset:3072
	s_waitcnt lgkmcnt(3)
	v_mfma_f32_16x16x32_bf16 v[6:9], v[10:13], v[18:21], 0
	s_mov_b32 s8, 0x43998000
	s_waitcnt lgkmcnt(0)
	v_mfma_f32_16x16x32_bf16 v[10:13], v[2:5], v[86:89], v[6:9]
	ds_read_b128 v[2:5], v80 offset:5120
	v_mfma_f32_16x16x32_bf16 v[6:9], v[70:73], v[18:21], 0
	ds_read_b128 v[70:73], v80 offset:7168
	s_waitcnt lgkmcnt(1)
	v_mfma_f32_16x16x32_bf16 v[6:9], v[2:5], v[86:89], v[6:9]
	v_mfma_f32_16x16x32_bf16 v[2:5], v[74:77], v[18:21], 0
	v_mov_b32_e32 v18, 0x23e10
	ds_read_b128 v[98:101], v1
	ds_read_b128 v[18:21], v18
	v_add_u32_e32 v1, s46, v80
	s_waitcnt vmcnt(11)
	ds_write_b128 v1, v[22:25]
	s_waitcnt vmcnt(10)
	ds_write_b128 v1, v[62:65] offset:1024
	s_waitcnt vmcnt(9)
	ds_write_b128 v1, v[66:69] offset:2048
	s_waitcnt lgkmcnt(5)
	v_mfma_f32_16x16x32_bf16 v[2:5], v[70:73], v[86:89], v[2:5]
	ds_read2_b32 v[88:89], v96 offset1:12
	ds_read2_b32 v[90:91], v96 offset0:24 offset1:36
	ds_read2_b32 v[86:87], v96 offset0:192 offset1:204
	ds_read2_b32 v[82:83], v96 offset0:216 offset1:228
	v_add_u32_e32 v63, 0x400, v96
	ds_read2_b32 v[66:67], v63 offset0:128 offset1:140
	ds_read2_b32 v[68:69], v63 offset0:152 offset1:164
	v_add_u32_e32 v62, 0x800, v96
	ds_read_b128 v[22:25], v80 offset:8192
	ds_read2_b32 v[94:95], v62 offset0:64 offset1:76
	ds_read2_b32 v[92:93], v62 offset0:88 offset1:100
	ds_read_b128 v[106:109], v80 offset:9216
	s_waitcnt lgkmcnt(9)
	v_cvt_pk_bf16_f32 v102, v88, v89
	s_waitcnt lgkmcnt(8)
	v_cvt_pk_bf16_f32 v103, v90, v91
	s_waitcnt lgkmcnt(7)
	v_cvt_pk_bf16_f32 v104, v86, v87
	s_waitcnt lgkmcnt(6)
	v_cvt_pk_bf16_f32 v105, v82, v83
	s_waitcnt lgkmcnt(5)
	v_cvt_pk_bf16_f32 v110, v66, v67
	s_waitcnt lgkmcnt(4)
	v_cvt_pk_bf16_f32 v111, v68, v69
	s_waitcnt lgkmcnt(3)
	v_mfma_f32_16x16x32_bf16 v[22:25], v[22:25], v[102:105], v[98:101]
	s_waitcnt lgkmcnt(2)
	v_cvt_pk_bf16_f32 v112, v94, v95
	s_waitcnt lgkmcnt(1)
	v_cvt_pk_bf16_f32 v113, v92, v93
	s_waitcnt lgkmcnt(0)
	s_nop 0
	v_mfma_f32_16x16x32_bf16 v[22:25], v[106:109], v[110:113], v[22:25]
	s_mul_i32 s58, s37, 0xc00
	v_add_u32_e32 v133, s58, v80
	global_load_dwordx4 v[136:139], v133, s[28:29]
	global_load_dwordx4 v[140:143], v133, s[28:29] offset:1024
	global_load_dwordx4 v[144:147], v133, s[28:29] offset:2048
	global_load_dwordx4 v[148:151], v133, s[30:31]
	global_load_dwordx4 v[156:159], v133, s[30:31] offset:1024
	global_load_dwordx4 v[160:163], v133, s[30:31] offset:2048
	s_cbranch_scc1 .LBB5_209
	s_waitcnt vmcnt(14)
	ds_write_b128 v1, v[50:53]
	s_waitcnt vmcnt(13)
	ds_write_b128 v1, v[54:57] offset:1024
	s_waitcnt vmcnt(12)
	ds_write_b128 v1, v[58:61] offset:2048
	ds_read2_b32 v[54:55], v96 offset1:12
	ds_read2_b32 v[56:57], v96 offset0:24 offset1:36
	ds_read2_b32 v[64:65], v96 offset0:192 offset1:204
	ds_read2_b32 v[98:99], v96 offset0:216 offset1:228
	ds_read2_b32 v[100:101], v63 offset0:128 offset1:140
	ds_read2_b32 v[102:103], v63 offset0:152 offset1:164
	ds_read2_b32 v[104:105], v62 offset0:64 offset1:76
	ds_read_b128 v[50:53], v80
	ds_read2_b32 v[106:107], v62 offset0:88 offset1:100
	ds_read_b128 v[58:61], v80 offset:1024
	s_waitcnt lgkmcnt(9)
	v_cvt_pk_bf16_f32 v54, v54, v55
	s_waitcnt lgkmcnt(8)
	v_cvt_pk_bf16_f32 v55, v56, v57
	s_waitcnt lgkmcnt(7)
	v_cvt_pk_bf16_f32 v56, v64, v65
	s_waitcnt lgkmcnt(6)
	v_cvt_pk_bf16_f32 v57, v98, v99
	s_waitcnt lgkmcnt(5)
	v_cvt_pk_bf16_f32 v62, v100, v101
	ds_read_b128 v[98:101], v80 offset:2048
	s_waitcnt lgkmcnt(3)
	v_mfma_f32_16x16x32_bf16 v[50:53], v[50:53], v[54:57], 0
	v_cvt_pk_bf16_f32 v63, v102, v103
	v_cvt_pk_bf16_f32 v64, v104, v105
	s_waitcnt lgkmcnt(2)
	v_cvt_pk_bf16_f32 v65, v106, v107
	s_waitcnt lgkmcnt(0)
	v_mfma_f32_16x16x32_bf16 v[98:101], v[98:101], v[54:57], 0
	ds_read_b128 v[102:105], v80 offset:4096
	ds_read_b128 v[106:109], v80 offset:11264
	v_mfma_f32_16x16x32_bf16 v[50:53], v[58:61], v[62:65], v[50:53]
	ds_read_b128 v[58:61], v80 offset:3072
	s_waitcnt lgkmcnt(0)
	v_mfma_f32_16x16x32_bf16 v[58:61], v[58:61], v[62:65], v[98:101]
	s_nop 2
	ds_read_b128 v[98:101], v80 offset:5120
	v_mfma_f32_16x16x32_bf16 v[102:105], v[102:105], v[54:57], 0
	s_waitcnt lgkmcnt(0)
	v_mfma_f32_16x16x32_bf16 v[98:101], v[98:101], v[62:65], v[102:105]
	s_nop 5
	ds_read_b128 v[102:105], v80 offset:10240
	v_mfma_f32_16x16x32_bf16 v[74:77], v[74:77], v[54:57], 0
	s_waitcnt lgkmcnt(0)
	v_mfma_f32_16x16x32_bf16 v[54:57], v[102:105], v[54:57], v[18:21]
	v_mfma_f32_16x16x32_bf16 v[54:57], v[106:109], v[62:65], v[54:57]
	v_mfma_f32_16x16x32_bf16 v[62:65], v[70:73], v[62:65], v[74:77]
	s_nop 6
	v_add_f32_e32 v54, v22, v54
	v_mul_f32_e32 v81, 0x3e4ccccd, v54
	v_cmp_lt_f32_e32 vcc, 0, v54
	v_add_f32_e32 v55, v23, v55
	v_mul_f32_e32 v97, 0x3e4ccccd, v55
	v_cndmask_b32_e32 v54, v81, v54, vcc
	v_cmp_lt_f32_e32 vcc, 0, v55
	v_mov_b32_e32 v81, s18
	v_fma_f32 v54, s15, v54, v81
	v_cndmask_b32_e32 v55, v97, v55, vcc
	v_fma_f32 v55, s15, v55, v81
	v_mul_f32_e32 v54, 0x3fb8aa3b, v54
	v_mul_f32_e32 v55, 0x3fb8aa3b, v55
	v_exp_f32_e32 v54, v54
	v_exp_f32_e32 v55, v55
	s_nop 0
	v_pk_add_f32 v[54:55], v[54:55], -1.0 op_sel_hi:[1,0]
	s_nop 0
	v_pk_fma_f32 v[16:17], v[52:53], v[54:55], v[16:17] op_sel_hi:[1,0,1]
	v_add_f32_e32 v52, v24, v56
	v_mul_f32_e32 v53, 0x3e4ccccd, v52
	v_cmp_lt_f32_e32 vcc, 0, v52
	v_pk_fma_f32 v[14:15], v[50:51], v[54:55], v[14:15] op_sel_hi:[1,0,1]
	v_pk_fma_f32 v[12:13], v[60:61], v[54:55], v[12:13] op_sel:[0,1,0]
	v_cndmask_b32_e32 v52, v53, v52, vcc
	v_add_f32_e32 v53, v25, v57
	v_mul_f32_e32 v56, 0x3e4ccccd, v53
	v_cmp_lt_f32_e32 vcc, 0, v53
	v_fma_f32 v52, s15, v52, v81
	v_mul_f32_e32 v52, 0x3fb8aa3b, v52
	v_cndmask_b32_e32 v53, v56, v53, vcc
	v_fma_f32 v53, s15, v53, v81
	v_mul_f32_e32 v53, 0x3fb8aa3b, v53
	v_exp_f32_e32 v52, v52
	v_exp_f32_e32 v53, v53
	v_pk_fma_f32 v[10:11], v[58:59], v[54:55], v[10:11] op_sel:[0,1,0]
	v_pk_add_f32 v[72:73], v[54:55], s[8:9] op_sel_hi:[1,0]
	v_pk_add_f32 v[50:51], v[52:53], -1.0 op_sel_hi:[1,0]
	s_nop 0
	v_pk_fma_f32 v[8:9], v[100:101], v[50:51], v[8:9] op_sel_hi:[1,0,1]
	v_pk_fma_f32 v[6:7], v[98:99], v[50:51], v[6:7] op_sel_hi:[1,0,1]
	v_pk_add_f32 v[70:71], v[50:51], s[8:9] op_sel_hi:[1,0]
	v_pk_fma_f32 v[4:5], v[64:65], v[50:51], v[4:5] op_sel:[0,1,0]
	v_pk_fma_f32 v[2:3], v[62:63], v[50:51], v[2:3] op_sel:[0,1,0]
	s_cmp_lt_i32 s48, 2
	s_cbranch_scc1 .LBB5_87
